# dsa tile loop: waves 4-7 start each tile step 512 cycles late (s_sleep 8) so their QK MFMAs overlap the other half's softmax VALU
# baseline (speedup 1.0000x reference)
.LBB0_1218:
	v_readfirstlane_b32 s100, v0
	s_bitcmp1_b32 s100, 8
	s_cbranch_scc0 .Ldsa_nostag
	s_sleep 8
